# v12: inproj start stagger shortened from 127 to 8 sleep units per group
# speedup vs baseline: 1.0201x; 1.0015x over previous
.LBB0_535:
	s_add_i32 s0, s0, -1
	s_cmp_eq_u32 s0, 0
	s_sleep 0x08
	s_cbranch_scc0 .LBB0_535
